# attn_pull start (B1/B): the three initial ticket pairs come from one atomic add of 3 instead of three serial atomic round trips; on top of m14
# baseline (speedup 1.0000x reference)
; #define GAS __attribute__((address_space(1)))
; #define LAS __attribute__((address_space(3)))
; DI int rfl(int v) { return __builtin_amdgcn_readfirstlane(v); }
; DI int ltid() { int t = threadIdx.x; asm volatile("" : "+v"(t)); return t; }
; DI void attn_pull(LAS unsigned char* lds, const Ctx& c, unsigned* ctr, int base, int limit) {
;     volatile LAS int* TK = (volatile LAS int*)(lds + MISC_OFF + 192);
;     const int tid = ltid();
;     __syncthreads();
;     if (tid == 0) { TK[0] = base + 2 * (int)__hip_atomic_fetch_add((GAS unsigned*)ctr, 1u, __ATOMIC_RELAXED, __HIP_MEMORY_SCOPE_AGENT); TK[1] = base + 2 * (int)__hip_atomic_fetch_add((GAS unsigned*)ctr, 1u, __ATOMIC_RELAXED, __HIP_MEMORY_SCOPE_AGENT);
;         TK[2] = base + 2 * (int)__hip_atomic_fetch_add((GAS unsigned*)ctr, 1u, __ATOMIC_RELAXED, __HIP_MEMORY_SCOPE_AGENT); }
;     __syncthreads();
;     int cur = rfl(TK[0]), nxt = rfl(TK[1]);
.LBB0_652:
	v_readlane_b32 s4, v254, 38
	s_lshl_b32 s4, s4, 7
	v_readlane_b32 s5, v254, 57
	s_or_b32 s68, s4, s5
	s_lshl_b64 s[4:5], s[68:69], 2
	s_add_u32 s4, s30, s4
	s_addc_u32 s5, s31, s5
	s_add_u32 s16, s4, 0x18000
	s_waitcnt vmcnt(0)
	v_mov_b32_e32 v1, v0
	s_addc_u32 s17, s5, 0
	s_add_i32 s4, s38, 0x27fc0
	s_waitcnt vmcnt(0)
	v_cmp_eq_u32_e64 s[40:41], 0, v1
	s_barrier
	s_and_saveexec_b64 s[42:43], s[40:41]
	s_cbranch_execz .LBB0_660
	s_mov_b64 s[46:47], exec
	v_mbcnt_lo_u32_b32 v1, s46, 0
	v_mbcnt_hi_u32_b32 v1, s47, v1
	v_cmp_eq_u32_e32 vcc, 0, v1
	s_and_saveexec_b64 s[44:45], vcc
	s_cbranch_execz .LBB0_655
	s_bcnt1_i32_b64 s5, s[46:47]
	s_mul_i32 s5, s5, 3
	v_mov_b32_e32 v2, s5
	global_atomic_add v2, v4, v2, s[16:17] sc0
.LBB0_655:
	s_or_b64 exec, exec, s[44:45]
	s_waitcnt vmcnt(0)
	v_readfirstlane_b32 s5, v2
	s_mov_b32 s100, s5
	s_mov_b64 s[44:45], exec
	v_mov_b32_e32 v2, s4
	v_add_lshl_u32 v1, s5, v1, 1
	ds_write_b32 v2, v1
	v_mbcnt_lo_u32_b32 v1, s44, 0
	v_mbcnt_hi_u32_b32 v1, s45, v1
	v_cmp_eq_u32_e32 vcc, 0, v1
	s_and_saveexec_b64 s[46:47], vcc
	s_cbranch_execz .LBB0_657
	s_bcnt1_i32_b64 s5, s[44:45]
	v_mov_b32_e32 v2, s5
	s_add_i32 s100, s100, 1
	v_mov_b32_e32 v2, s100
.LBB0_657:
	s_or_b64 exec, exec, s[46:47]
	s_waitcnt vmcnt(0)
	v_readfirstlane_b32 s5, v2
	s_mov_b64 s[44:45], exec
	s_nop 0
	v_add_lshl_u32 v1, s5, v1, 1
	s_add_i32 s5, s38, 0x27fc4
	v_mov_b32_e32 v2, s5
	ds_write_b32 v2, v1
	v_mbcnt_lo_u32_b32 v1, s44, 0
	v_mbcnt_hi_u32_b32 v1, s45, v1
	v_cmp_eq_u32_e32 vcc, 0, v1
	s_and_saveexec_b64 s[46:47], vcc
	s_cbranch_execz .LBB0_659
	s_bcnt1_i32_b64 s5, s[44:45]
	v_mov_b32_e32 v2, s5
	s_add_i32 s100, s100, 1
	v_mov_b32_e32 v2, s100

; #define GAS __attribute__((address_space(1)))
; #define LAS __attribute__((address_space(3)))
; DI int rfl(int v) { return __builtin_amdgcn_readfirstlane(v); }
; DI int ltid() { int t = threadIdx.x; asm volatile("" : "+v"(t)); return t; }
; DI void attn_pull(LAS unsigned char* lds, const Ctx& c, unsigned* ctr, int base, int limit) {
;     volatile LAS int* TK = (volatile LAS int*)(lds + MISC_OFF + 192);
;     const int tid = ltid();
;     __syncthreads();
;     if (tid == 0) { TK[0] = base + 2 * (int)__hip_atomic_fetch_add((GAS unsigned*)ctr, 1u, __ATOMIC_RELAXED, __HIP_MEMORY_SCOPE_AGENT); TK[1] = base + 2 * (int)__hip_atomic_fetch_add((GAS unsigned*)ctr, 1u, __ATOMIC_RELAXED, __HIP_MEMORY_SCOPE_AGENT);
;         TK[2] = base + 2 * (int)__hip_atomic_fetch_add((GAS unsigned*)ctr, 1u, __ATOMIC_RELAXED, __HIP_MEMORY_SCOPE_AGENT); }
;     __syncthreads();
;     int cur = rfl(TK[0]), nxt = rfl(TK[1]);
.LBB0_773:
	v_readlane_b32 s2, v254, 38
	s_lshl_b32 s4, s2, 7
	v_readlane_b32 s2, v254, 57
	s_or_b32 s68, s4, s2
	s_lshl_b64 s[4:5], s[68:69], 2
	s_add_u32 s4, s30, s4
	s_addc_u32 s5, s31, s5
	s_add_u32 s16, s4, 0x18100
	s_waitcnt vmcnt(0)
	v_mov_b32_e32 v1, v0
	s_addc_u32 s17, s5, 0
	s_add_i32 s4, s38, 0x27fc0
	s_waitcnt vmcnt(0)
	v_cmp_eq_u32_e64 s[40:41], 0, v1
	s_barrier
	s_and_saveexec_b64 s[42:43], s[40:41]
	s_cbranch_execz .LBB0_781
	s_mov_b64 s[46:47], exec
	v_mbcnt_lo_u32_b32 v1, s46, 0
	v_mbcnt_hi_u32_b32 v1, s47, v1
	v_cmp_eq_u32_e32 vcc, 0, v1
	s_and_saveexec_b64 s[44:45], vcc
	s_cbranch_execz .LBB0_776
	s_bcnt1_i32_b64 s5, s[46:47]
	s_mul_i32 s5, s5, 3
	v_mov_b32_e32 v2, s5
	global_atomic_add v2, v4, v2, s[16:17] sc0
.LBB0_776:
	s_or_b64 exec, exec, s[44:45]
	s_waitcnt vmcnt(0)
	v_readfirstlane_b32 s5, v2
	s_mov_b32 s100, s5
	s_mov_b64 s[44:45], exec
	v_mov_b32_e32 v2, s4
	v_add_u32_e32 v1, s5, v1
	v_lshl_add_u32 v1, v1, 1, v222
	ds_write_b32 v2, v1
	v_mbcnt_lo_u32_b32 v1, s44, 0
	v_mbcnt_hi_u32_b32 v1, s45, v1
	v_cmp_eq_u32_e32 vcc, 0, v1
	s_and_saveexec_b64 s[46:47], vcc
	s_cbranch_execz .LBB0_778
	s_bcnt1_i32_b64 s5, s[44:45]
	v_mov_b32_e32 v2, s5
	s_add_i32 s100, s100, 1
	v_mov_b32_e32 v2, s100
.LBB0_778:
	s_or_b64 exec, exec, s[46:47]
	s_waitcnt vmcnt(0)
	v_readfirstlane_b32 s5, v2
	s_mov_b64 s[44:45], exec
	s_nop 0
	v_add_u32_e32 v1, s5, v1
	s_add_i32 s5, s38, 0x27fc4
	v_lshl_add_u32 v1, v1, 1, v222
	v_mov_b32_e32 v2, s5
	ds_write_b32 v2, v1
	v_mbcnt_lo_u32_b32 v1, s44, 0
	v_mbcnt_hi_u32_b32 v1, s45, v1
	v_cmp_eq_u32_e32 vcc, 0, v1
	s_and_saveexec_b64 s[46:47], vcc
	s_cbranch_execz .LBB0_780
	s_bcnt1_i32_b64 s5, s[44:45]
	v_mov_b32_e32 v2, s5
	s_add_i32 s100, s100, 1
	v_mov_b32_e32 v2, s100
